# P12: store drain hoisted out of the loop plus nt on the read-once H-row loads (both on the chunk-136 split with P1-tail conversion blocks)
# speedup vs baseline: 1.0012x; 1.0000x over previous
; #define GAS __attribute__((address_space(1)))
; #define LAS __attribute__((address_space(3)))
; __global__ void __launch_bounds__(NTHR, 2) mk_fwd(Args args) {
;     ...
;         LAS float* s_lnw = (LAS float*)lds; LAS float* s_lnb = s_lnw + 2048;
;         *(LAS f32x4*)(s_lnw + 4 * tid) = *(const GAS f32x4*)(ln2_w + 4 * tid); *(LAS f32x4*)(s_lnb + 4 * tid) = *(const GAS f32x4*)(ln2_b + 4 * tid);
;         __syncthreads();
;         int nsl[4]; float ngt[4];
; #pragma unroll
;         for (int k = 0; k < 4; ++k) { nsl[k] = SLOT_OF[gw * 4 + k]; ngt[k] = GATE[gw * 4 + k]; }
; #pragma unroll 1
;         for (int m = gw; m < M; m += NGW) {
;             int sl[4]; float gt[4];
; #pragma unroll
;             for (int k = 0; k < 4; ++k) { sl[k] = nsl[k]; gt[k] = ngt[k]; }
;             { const int mn = m + NGW < M ? m + NGW : m;
; #pragma unroll
;               for (int k = 0; k < 4; ++k) { nsl[k] = SLOT_OF[mn * 4 + k]; ngt[k] = GATE[mn * 4 + k]; } }
;             f32x4 v[8]; float s = 0.f;
; #pragma unroll
;             for (int q = 0; q < 8; ++q) { const int c = 4 * lane + 256 * q; f32x4 f = (f32x4){0.f, 0.f, 0.f, 0.f};
; #pragma unroll
;                 for (int k = 0; k < 4; ++k) { const unsigned yv = *(const GAS unsigned*)(YS + (size_t)sl[k] * D + c); const f32x2n lo2 = __builtin_amdgcn_cvt_pk_f32_fp8(yv, false), hi2 = __builtin_amdgcn_cvt_pk_f32_fp8(yv, true); f += (gt[k] * (1.0f / pg8::YS_SCALE)) * (f32x4){lo2.x, lo2.y, hi2.x, hi2.y}; }
;                 { const v2u hw = *(const GAS v2u*)(H + (size_t)m * D + c); v[q] = ALPHA * (f32x4){bflo(hw.x), bfhi(hw.x), bflo(hw.y), bfhi(hw.y)} + f; } s += (v[q].x + v[q].y) + (v[q].z + v[q].w); }
.LBB0_1219:
	v_ashrrev_i32_e32 v97, 31, v64
	v_mov_b32_e32 v96, v64
	v_ashrrev_i32_e32 v99, 31, v65
	v_mov_b32_e32 v98, v65
	v_ashrrev_i32_e32 v101, 31, v66
	v_mov_b32_e32 v100, v66
	v_ashrrev_i32_e32 v103, 31, v67
	v_mov_b32_e32 v102, v67
	v_lshlrev_b64 v[96:97], 11, v[96:97]
	v_lshlrev_b64 v[98:99], 11, v[98:99]
	v_lshlrev_b64 v[100:101], 11, v[100:101]
	v_lshlrev_b64 v[102:103], 11, v[102:103]
	v_lshl_add_u64 v[124:125], v[74:75], 0, v[96:97]
	v_lshl_add_u64 v[96:97], s[8:9], 0, v[96:97]
	v_mul_f32_e32 v94, 0x3d800000, v68
	v_mul_f32_e32 v92, 0x3d800000, v69
	v_mul_f32_e32 v64, 0x3d800000, v70
	v_mul_f32_e32 v68, 0x3d800000, v71
	global_load_dwordx2 v[66:67], v[90:91], off nt
	global_load_dwordx2 v[70:71], v[90:91], off offset:512 nt
	global_load_dwordx2 v[104:105], v[90:91], off offset:1024 nt
	global_load_dwordx2 v[108:109], v[90:91], off offset:1536 nt
	global_load_dwordx2 v[110:111], v[90:91], off offset:2048 nt
	global_load_dwordx2 v[112:113], v[90:91], off offset:2560 nt
	global_load_dwordx2 v[114:115], v[90:91], off offset:3072 nt
	global_load_dwordx2 v[116:117], v[90:91], off offset:3584 nt
	v_lshl_add_u64 v[126:127], v[74:75], 0, v[98:99]
	v_lshl_add_u64 v[128:129], v[74:75], 0, v[100:101]
	v_lshl_add_u64 v[130:131], v[74:75], 0, v[102:103]
	global_load_dword v65, v[124:125], off
	global_load_dword v69, v[126:127], off
	global_load_dword v172, v[128:129], off
	global_load_dword v173, v[130:131], off
	v_lshl_add_u64 v[124:125], v[96:97], 0, v[72:73]
	s_add_i32 s0, s30, s28
	global_load_dword v174, v[124:125], off
	s_cmpk_lt_i32 s0, 0x4000
	s_cselect_b64 s[2:3], -1, 0
	s_and_b64 s[16:17], s[2:3], exec
	s_cselect_b32 s1, s0, s30
	v_lshl_add_u64 v[98:99], s[8:9], 0, v[98:99]
	s_mov_b32 s30, s0
	s_lshl_b32 s0, s1, 2
	v_lshl_add_u64 v[100:101], s[8:9], 0, v[100:101]
	v_lshl_add_u64 v[102:103], s[8:9], 0, v[102:103]
	v_lshl_add_u64 v[126:127], v[98:99], 0, v[72:73]
	s_ashr_i32 s1, s0, 31
	v_lshl_add_u64 v[128:129], v[100:101], 0, v[72:73]
	v_lshl_add_u64 v[130:131], v[102:103], 0, v[72:73]
	v_lshl_add_u64 v[132:133], v[96:97], 0, v[76:77]
	v_lshl_add_u64 v[134:135], v[98:99], 0, v[76:77]
	v_lshl_add_u64 v[136:137], v[100:101], 0, v[76:77]
	v_lshl_add_u64 v[138:139], v[102:103], 0, v[76:77]
	v_lshl_add_u64 v[140:141], v[96:97], 0, v[78:79]
	v_lshl_add_u64 v[142:143], v[98:99], 0, v[78:79]
	v_lshl_add_u64 v[144:145], v[100:101], 0, v[78:79]
	v_lshl_add_u64 v[146:147], v[102:103], 0, v[78:79]
	v_lshl_add_u64 v[148:149], v[96:97], 0, v[80:81]
	v_lshl_add_u64 v[150:151], v[98:99], 0, v[80:81]
	v_lshl_add_u64 v[152:153], v[100:101], 0, v[80:81]
	v_lshl_add_u64 v[154:155], v[102:103], 0, v[80:81]
	v_lshl_add_u64 v[156:157], v[96:97], 0, v[82:83]
	v_lshl_add_u64 v[158:159], v[98:99], 0, v[82:83]
	v_lshl_add_u64 v[160:161], v[100:101], 0, v[82:83]
	v_lshl_add_u64 v[162:163], v[102:103], 0, v[82:83]
	v_lshl_add_u64 v[164:165], v[96:97], 0, v[84:85]
	v_lshl_add_u64 v[166:167], v[98:99], 0, v[84:85]
	v_lshl_add_u64 v[168:169], v[100:101], 0, v[84:85]
	v_lshl_add_u64 v[170:171], v[102:103], 0, v[84:85]
	v_lshl_add_u64 v[96:97], v[96:97], 0, v[86:87]
	v_lshl_add_u64 v[98:99], v[98:99], 0, v[86:87]
	v_lshl_add_u64 v[100:101], v[100:101], 0, v[86:87]
	v_lshl_add_u64 v[102:103], v[102:103], 0, v[86:87]
	global_load_dword v175, v[126:127], off
	global_load_dword v176, v[128:129], off
	global_load_dword v177, v[130:131], off
	global_load_dword v178, v[132:133], off
	global_load_dword v179, v[134:135], off
	global_load_dword v182, v[136:137], off
	global_load_dword v186, v[138:139], off
	global_load_dword v190, v[140:141], off
	global_load_dword v194, v[142:143], off
	global_load_dword v198, v[144:145], off
	global_load_dword v202, v[146:147], off
	global_load_dword v206, v[148:149], off
	global_load_dword v210, v[150:151], off
	global_load_dword v214, v[152:153], off
	global_load_dword v218, v[154:155], off
	global_load_dword v222, v[156:157], off
	global_load_dword v226, v[158:159], off
	global_load_dword v230, v[160:161], off
	global_load_dword v234, v[162:163], off
	global_load_dword v238, v[164:165], off
	global_load_dword v242, v[166:167], off
	global_load_dword v246, v[168:169], off
	global_load_dword v248, v[170:171], off
	global_load_dword v244, v[96:97], off
	global_load_dword v249, v[98:99], off
	global_load_dword v250, v[100:101], off
	global_load_dword v251, v[102:103], off
	s_lshl_b64 s[0:1], s[0:1], 2
	s_add_u32 s16, s4, s0
	s_addc_u32 s17, s5, s1
	global_load_dwordx4 v[96:99], v73, s[16:17]
	s_add_u32 s18, s66, s0
	s_addc_u32 s19, s67, s1
	global_load_dwordx4 v[100:103], v73, s[18:19]
	v_mov_b32_e32 v120, 0
	v_mov_b32_e32 v121, 0
	s_and_b64 s[0:1], s[2:3], exec
	v_mov_b32_e32 v122, 0
	v_mov_b32_e32 v123, 0
	v_add_co_u32_e32 v106, vcc, s14, v88
	v_lshl_add_u64 v[90:91], v[90:91], 0, s[10:11]
	s_nop 0
	v_addc_co_u32_e32 v107, vcc, -1, v89, vcc
	s_waitcnt vmcnt(41)
	v_lshlrev_b32_e32 v124, 16, v66
	v_and_b32_e32 v125, 0xffff0000, v66
	v_lshlrev_b32_e32 v126, 16, v67
	v_and_b32_e32 v127, 0xffff0000, v67
	s_waitcnt vmcnt(40)
	v_lshlrev_b32_e32 v128, 16, v70
	v_and_b32_e32 v129, 0xffff0000, v70
	v_lshlrev_b32_e32 v70, 16, v71
	v_and_b32_e32 v71, 0xffff0000, v71
	s_waitcnt vmcnt(33)
	v_cvt_pk_f32_fp8_e32 v[66:67], v65
	v_cvt_pk_f32_fp8_sdwa v[142:143], v65 src0_sel:WORD_1
	s_waitcnt vmcnt(32)
	v_cvt_pk_f32_fp8_e32 v[144:145], v69
	v_cvt_pk_f32_fp8_sdwa v[146:147], v69 src0_sel:WORD_1
	s_waitcnt vmcnt(31)
	v_cvt_pk_f32_fp8_e32 v[148:149], v172
	v_cvt_pk_f32_fp8_sdwa v[150:151], v172 src0_sel:WORD_1
	s_waitcnt vmcnt(29)
; #define GAS __attribute__((address_space(1)))
; __global__ void __launch_bounds__(NTHR, 2) mk_fwd(Args args) {
;     ...
;             { const int mn = m + NGW < M ? m + NGW : m;
; #pragma unroll
;               for (int k = 0; k < 4; ++k) { nsl[k] = SLOT_OF[mn * 4 + k]; ngt[k] = GATE[mn * 4 + k]; } }
;             f32x4 v[8]; float s = 0.f;
; #pragma unroll
;             for (int q = 0; q < 8; ++q) { const int c = 4 * lane + 256 * q; f32x4 f = (f32x4){0.f, 0.f, 0.f, 0.f};
; #pragma unroll
;                 for (int k = 0; k < 4; ++k) { const unsigned yv = *(const GAS unsigned*)(YS + (size_t)sl[k] * D + c); const f32x2n lo2 = __builtin_amdgcn_cvt_pk_f32_fp8(yv, false), hi2 = __builtin_amdgcn_cvt_pk_f32_fp8(yv, true); f += (gt[k] * (1.0f / pg8::YS_SCALE)) * (f32x4){lo2.x, lo2.y, hi2.x, hi2.y}; }
	v_cvt_pk_f32_fp8_e32 v[156:157], v174
	v_cvt_pk_f32_fp8_e32 v[152:153], v173
	v_cvt_pk_f32_fp8_sdwa v[154:155], v173 src0_sel:WORD_1
	v_cvt_pk_f32_fp8_sdwa v[158:159], v174 src0_sel:WORD_1
	v_pk_fma_f32 v[66:67], v[66:67], v[94:95], 0 op_sel_hi:[1,0,0]
	v_pk_fma_f32 v[142:143], v[142:143], v[94:95], 0 op_sel_hi:[1,0,0]
	v_pk_fma_f32 v[66:67], v[144:145], v[92:93], v[66:67] op_sel_hi:[1,0,1]
	v_pk_fma_f32 v[142:143], v[146:147], v[92:93], v[142:143] op_sel_hi:[1,0,1]
	v_pk_fma_f32 v[156:157], v[156:157], v[94:95], 0 op_sel_hi:[1,0,0]
	v_pk_fma_f32 v[158:159], v[158:159], v[94:95], 0 op_sel_hi:[1,0,0]
	v_pk_fma_f32 v[142:143], v[150:151], v[64:65], v[142:143] op_sel_hi:[1,0,1]
	v_pk_fma_f32 v[66:67], v[148:149], v[64:65], v[66:67] op_sel_hi:[1,0,1]
	s_waitcnt vmcnt(28)
	v_cvt_pk_f32_fp8_e32 v[160:161], v175
	v_cvt_pk_f32_fp8_sdwa v[162:163], v175 src0_sel:WORD_1
	s_waitcnt vmcnt(27)
	v_cvt_pk_f32_fp8_e32 v[164:165], v176
	s_waitcnt vmcnt(25)
	v_cvt_pk_f32_fp8_e32 v[172:173], v178
	v_cvt_pk_f32_fp8_sdwa v[166:167], v176 src0_sel:WORD_1
	v_cvt_pk_f32_fp8_e32 v[168:169], v177
	v_cvt_pk_f32_fp8_sdwa v[170:171], v177 src0_sel:WORD_1
	s_waitcnt vmcnt(24)
	v_cvt_pk_f32_fp8_e32 v[176:177], v179
	v_cvt_pk_f32_fp8_sdwa v[174:175], v178 src0_sel:WORD_1
	v_cvt_pk_f32_fp8_sdwa v[178:179], v179 src0_sel:WORD_1
	s_waitcnt vmcnt(21)
	v_cvt_pk_f32_fp8_e32 v[188:189], v190
	v_cvt_pk_f32_fp8_sdwa v[190:191], v190 src0_sel:WORD_1
	s_waitcnt vmcnt(17)
	v_cvt_pk_f32_fp8_e32 v[204:205], v206
	v_cvt_pk_f32_fp8_sdwa v[206:207], v206 src0_sel:WORD_1
	v_cvt_pk_f32_fp8_e32 v[192:193], v194
	s_waitcnt vmcnt(13)
	v_cvt_pk_f32_fp8_e32 v[220:221], v222
	v_cvt_pk_f32_fp8_sdwa v[222:223], v222 src0_sel:WORD_1
	v_cvt_pk_f32_fp8_sdwa v[194:195], v194 src0_sel:WORD_1
	v_cvt_pk_f32_fp8_e32 v[208:209], v210
	s_waitcnt vmcnt(9)
	v_cvt_pk_f32_fp8_e32 v[236:237], v238
	v_cvt_pk_f32_fp8_sdwa v[238:239], v238 src0_sel:WORD_1
	v_cvt_pk_f32_fp8_sdwa v[210:211], v210 src0_sel:WORD_1
	v_cvt_pk_f32_fp8_e32 v[224:225], v226
	s_waitcnt vmcnt(5)
	v_cvt_pk_f32_fp8_e32 v[144:145], v244
	v_cvt_pk_f32_fp8_sdwa v[146:147], v244 src0_sel:WORD_1
	v_cvt_pk_f32_fp8_sdwa v[226:227], v226 src0_sel:WORD_1
	v_cvt_pk_f32_fp8_e32 v[240:241], v242
	v_cvt_pk_f32_fp8_sdwa v[242:243], v242 src0_sel:WORD_1
	v_pk_fma_f32 v[172:173], v[172:173], v[94:95], 0 op_sel_hi:[1,0,0]
	v_cvt_pk_f32_fp8_e32 v[150:151], v248
	v_cvt_pk_f32_fp8_sdwa v[148:149], v248 src0_sel:WORD_1
	v_pk_fma_f32 v[156:157], v[160:161], v[92:93], v[156:157] op_sel_hi:[1,0,1]
	s_waitcnt vmcnt(4)
	v_cvt_pk_f32_fp8_e32 v[160:161], v249
	v_cvt_pk_f32_fp8_sdwa v[248:249], v249 src0_sel:WORD_1
	v_cvt_pk_f32_fp8_e32 v[180:181], v182
	v_cvt_pk_f32_fp8_sdwa v[182:183], v182 src0_sel:WORD_1
	v_cvt_pk_f32_fp8_e32 v[196:197], v198
	v_cvt_pk_f32_fp8_sdwa v[198:199], v198 src0_sel:WORD_1
	v_cvt_pk_f32_fp8_e32 v[212:213], v214
	v_cvt_pk_f32_fp8_sdwa v[214:215], v214 src0_sel:WORD_1
	v_cvt_pk_f32_fp8_e32 v[228:229], v230
	v_cvt_pk_f32_fp8_sdwa v[230:231], v230 src0_sel:WORD_1
	v_cvt_pk_f32_fp8_e32 v[244:245], v246
	v_cvt_pk_f32_fp8_sdwa v[246:247], v246 src0_sel:WORD_1
	v_pk_fma_f32 v[158:159], v[162:163], v[92:93], v[158:159] op_sel_hi:[1,0,1]
	s_waitcnt vmcnt(3)
	v_cvt_pk_f32_fp8_e32 v[162:163], v250
	v_pk_fma_f32 v[172:173], v[176:177], v[92:93], v[172:173] op_sel_hi:[1,0,1]
	v_cvt_pk_f32_fp8_sdwa v[176:177], v250 src0_sel:WORD_1
	v_cvt_pk_f32_fp8_e32 v[184:185], v186
	v_cvt_pk_f32_fp8_sdwa v[186:187], v186 src0_sel:WORD_1
	v_pk_fma_f32 v[174:175], v[174:175], v[94:95], 0 op_sel_hi:[1,0,0]
	v_cvt_pk_f32_fp8_e32 v[200:201], v202
	v_cvt_pk_f32_fp8_sdwa v[202:203], v202 src0_sel:WORD_1
	v_cvt_pk_f32_fp8_e32 v[216:217], v218
	v_cvt_pk_f32_fp8_sdwa v[218:219], v218 src0_sel:WORD_1
	v_cvt_pk_f32_fp8_e32 v[232:233], v234
	v_cvt_pk_f32_fp8_sdwa v[234:235], v234 src0_sel:WORD_1
	v_pk_fma_f32 v[190:191], v[190:191], v[94:95], 0 op_sel_hi:[1,0,0]
	v_pk_fma_f32 v[188:189], v[188:189], v[94:95], 0 op_sel_hi:[1,0,0]
	v_pk_fma_f32 v[206:207], v[206:207], v[94:95], 0 op_sel_hi:[1,0,0]
	v_pk_fma_f32 v[204:205], v[204:205], v[94:95], 0 op_sel_hi:[1,0,0]
	v_pk_fma_f32 v[222:223], v[222:223], v[94:95], 0 op_sel_hi:[1,0,0]
	v_pk_fma_f32 v[220:221], v[220:221], v[94:95], 0 op_sel_hi:[1,0,0]
	v_pk_fma_f32 v[238:239], v[238:239], v[94:95], 0 op_sel_hi:[1,0,0]
	v_pk_fma_f32 v[236:237], v[236:237], v[94:95], 0 op_sel_hi:[1,0,0]
	v_pk_fma_f32 v[146:147], v[146:147], v[94:95], 0 op_sel_hi:[1,0,0]
	v_pk_fma_f32 v[144:145], v[144:145], v[94:95], 0 op_sel_hi:[1,0,0]
	v_pk_fma_f32 v[174:175], v[178:179], v[92:93], v[174:175] op_sel_hi:[1,0,1]
	s_waitcnt vmcnt(2)
; #define GAS __attribute__((address_space(1)))
; __global__ void __launch_bounds__(NTHR, 2) mk_fwd(Args args) {
;     ...
;             for (int q = 0; q < 8; ++q) { const int c = 4 * lane + 256 * q; f32x4 f = (f32x4){0.f, 0.f, 0.f, 0.f};
; #pragma unroll
;                 for (int k = 0; k < 4; ++k) { const unsigned yv = *(const GAS unsigned*)(YS + (size_t)sl[k] * D + c); const f32x2n lo2 = __builtin_amdgcn_cvt_pk_f32_fp8(yv, false), hi2 = __builtin_amdgcn_cvt_pk_f32_fp8(yv, true); f += (gt[k] * (1.0f / pg8::YS_SCALE)) * (f32x4){lo2.x, lo2.y, hi2.x, hi2.y}; }
;                 { const v2u hw = *(const GAS v2u*)(H + (size_t)m * D + c); v[q] = ALPHA * (f32x4){bflo(hw.x), bfhi(hw.x), bflo(hw.y), bfhi(hw.y)} + f; } s += (v[q].x + v[q].y) + (v[q].z + v[q].w); }
	v_cvt_pk_f32_fp8_e32 v[178:179], v251
	v_cvt_pk_f32_fp8_sdwa v[250:251], v251 src0_sel:WORD_1
	v_pk_fma_f32 v[188:189], v[192:193], v[92:93], v[188:189] op_sel_hi:[1,0,1]
	v_pk_fma_f32 v[190:191], v[194:195], v[92:93], v[190:191] op_sel_hi:[1,0,1]
	v_pk_fma_f32 v[192:193], v[208:209], v[92:93], v[204:205] op_sel_hi:[1,0,1]
	v_pk_fma_f32 v[194:195], v[210:211], v[92:93], v[206:207] op_sel_hi:[1,0,1]
	v_pk_fma_f32 v[204:205], v[224:225], v[92:93], v[220:221] op_sel_hi:[1,0,1]
	v_pk_fma_f32 v[206:207], v[226:227], v[92:93], v[222:223] op_sel_hi:[1,0,1]
	v_pk_fma_f32 v[208:209], v[240:241], v[92:93], v[236:237] op_sel_hi:[1,0,1]
	v_pk_fma_f32 v[210:211], v[242:243], v[92:93], v[238:239] op_sel_hi:[1,0,1]
	v_pk_fma_f32 v[144:145], v[160:161], v[92:93], v[144:145] op_sel_hi:[1,0,1]
	v_pk_fma_f32 v[146:147], v[248:249], v[92:93], v[146:147] op_sel_hi:[1,0,1]
	v_pk_fma_f32 v[152:153], v[152:153], v[68:69], v[66:67] op_sel_hi:[1,0,1]
	v_pk_fma_f32 v[142:143], v[154:155], v[68:69], v[142:143] op_sel_hi:[1,0,1]
	v_pk_fma_f32 v[154:155], v[166:167], v[64:65], v[158:159] op_sel_hi:[1,0,1]
	v_pk_fma_f32 v[156:157], v[164:165], v[64:65], v[156:157] op_sel_hi:[1,0,1]
	v_pk_fma_f32 v[158:159], v[182:183], v[64:65], v[174:175] op_sel_hi:[1,0,1]
	v_pk_fma_f32 v[160:161], v[180:181], v[64:65], v[172:173] op_sel_hi:[1,0,1]
	v_pk_fma_f32 v[164:165], v[198:199], v[64:65], v[190:191] op_sel_hi:[1,0,1]
	v_pk_fma_f32 v[166:167], v[196:197], v[64:65], v[188:189] op_sel_hi:[1,0,1]
	v_pk_fma_f32 v[172:173], v[214:215], v[64:65], v[194:195] op_sel_hi:[1,0,1]
	v_pk_fma_f32 v[174:175], v[212:213], v[64:65], v[192:193] op_sel_hi:[1,0,1]
	v_pk_fma_f32 v[180:181], v[230:231], v[64:65], v[206:207] op_sel_hi:[1,0,1]
	v_pk_fma_f32 v[182:183], v[228:229], v[64:65], v[204:205] op_sel_hi:[1,0,1]
	v_pk_fma_f32 v[188:189], v[246:247], v[64:65], v[210:211] op_sel_hi:[1,0,1]
	v_pk_fma_f32 v[190:191], v[244:245], v[64:65], v[208:209] op_sel_hi:[1,0,1]
	v_pk_fma_f32 v[146:147], v[176:177], v[64:65], v[146:147] op_sel_hi:[1,0,1]
	v_pk_fma_f32 v[144:145], v[162:163], v[64:65], v[144:145] op_sel_hi:[1,0,1]
	s_waitcnt vmcnt(1)
	v_mov_b64_e32 v[66:67], v[98:99]
	v_mov_b64_e32 v[64:65], v[96:97]
	v_pk_fma_f32 v[96:97], v[126:127], s[12:13], v[142:143] op_sel_hi:[1,0,1]
	v_pk_fma_f32 v[98:99], v[124:125], s[12:13], v[152:153] op_sel_hi:[1,0,1]
	v_pk_fma_f32 v[124:125], v[168:169], v[68:69], v[156:157] op_sel_hi:[1,0,1]
	v_pk_fma_f32 v[126:127], v[170:171], v[68:69], v[154:155] op_sel_hi:[1,0,1]
	v_lshlrev_b32_e32 v130, 16, v104
	v_and_b32_e32 v131, 0xffff0000, v104
	v_lshlrev_b32_e32 v104, 16, v105
	v_and_b32_e32 v105, 0xffff0000, v105
	v_pk_fma_f32 v[142:143], v[184:185], v[68:69], v[160:161] op_sel_hi:[1,0,1]
	v_pk_fma_f32 v[152:153], v[186:187], v[68:69], v[158:159] op_sel_hi:[1,0,1]
	v_pk_fma_f32 v[126:127], v[70:71], s[12:13], v[126:127] op_sel_hi:[1,0,1]
	v_pk_fma_f32 v[124:125], v[128:129], s[12:13], v[124:125] op_sel_hi:[1,0,1]
	v_lshlrev_b32_e32 v140, 16, v116
	v_and_b32_e32 v141, 0xffff0000, v116
	v_lshlrev_b32_e32 v116, 16, v117
	v_and_b32_e32 v117, 0xffff0000, v117
	v_pk_fma_f32 v[154:155], v[200:201], v[68:69], v[166:167] op_sel_hi:[1,0,1]
	v_pk_fma_f32 v[156:157], v[202:203], v[68:69], v[164:165] op_sel_hi:[1,0,1]
	v_pk_fma_f32 v[158:159], v[216:217], v[68:69], v[174:175] op_sel_hi:[1,0,1]
	v_pk_fma_f32 v[160:161], v[218:219], v[68:69], v[172:173] op_sel_hi:[1,0,1]
	v_pk_fma_f32 v[162:163], v[232:233], v[68:69], v[182:183] op_sel_hi:[1,0,1]
	v_pk_fma_f32 v[164:165], v[234:235], v[68:69], v[180:181] op_sel_hi:[1,0,1]
	v_pk_fma_f32 v[150:151], v[150:151], v[68:69], v[190:191] op_sel_hi:[1,0,1]
	v_pk_fma_f32 v[148:149], v[148:149], v[68:69], v[188:189] op_sel_hi:[1,0,1]
	v_pk_fma_f32 v[144:145], v[178:179], v[68:69], v[144:145] op_sel_hi:[1,0,1]
	v_pk_fma_f32 v[68:69], v[250:251], v[68:69], v[146:147] op_sel_hi:[1,0,1]
	v_mov_b32_e32 v128, v98
	v_mov_b32_e32 v146, v99
	v_mov_b32_e32 v166, v96
	v_mov_b32_e32 v168, v97
	v_pk_fma_f32 v[104:105], v[104:105], s[12:13], v[152:153] op_sel_hi:[1,0,1]
	v_pk_fma_f32 v[130:131], v[130:131], s[12:13], v[142:143] op_sel_hi:[1,0,1]
	v_mov_b32_e32 v129, v124
	v_mov_b32_e32 v147, v125
	v_mov_b32_e32 v167, v126
	v_mov_b32_e32 v169, v127
	v_pk_fma_f32 v[116:117], v[116:117], s[12:13], v[68:69] op_sel_hi:[1,0,1]
	s_waitcnt vmcnt(0)
; #define GAS __attribute__((address_space(1)))
; __device__ __forceinline__ float wave_sum_dpp(float x) {
;     x = row16_sum(x);
;     x += __builtin_bit_cast(float, __builtin_amdgcn_update_dpp(0, __builtin_bit_cast(int, x), 0x142, 0xA, 0xF, false));
;     x += __builtin_bit_cast(float, __builtin_amdgcn_update_dpp(0, __builtin_bit_cast(int, x), 0x143, 0xC, 0xF, false));
;     return __builtin_bit_cast(float, __builtin_amdgcn_readlane(__builtin_bit_cast(int, x), 63));
; __global__ void __launch_bounds__(NTHR, 2) mk_fwd(Args args) {
;     ...
;                 { const v2u hw = *(const GAS v2u*)(H + (size_t)m * D + c); v[q] = ALPHA * (f32x4){bflo(hw.x), bfhi(hw.x), bflo(hw.y), bfhi(hw.y)} + f; } s += (v[q].x + v[q].y) + (v[q].z + v[q].w); }
;             const float mean = wave_sum_dpp(s) * (1.0f / D); float s2 = 0.f;
; #pragma unroll
;             for (int q = 0; q < 8; ++q) { v[q] = v[q] - mean; s2 += (v[q].x * v[q].x + v[q].y * v[q].y) + (v[q].z * v[q].z + v[q].w * v[q].w); }
	v_mov_b64_e32 v[70:71], v[102:103]
	v_mov_b64_e32 v[68:69], v[100:101]
	v_pk_mov_b32 v[100:101], v[130:131], v[104:105] op_sel:[1,0]
	v_mov_b32_e32 v102, v130
	v_mov_b32_e32 v103, v105
	v_pk_add_f32 v[128:129], v[128:129], v[146:147]
	v_pk_add_f32 v[146:147], v[166:167], v[168:169]
	v_lshlrev_b32_e32 v132, 16, v108
	v_and_b32_e32 v133, 0xffff0000, v108
	v_lshlrev_b32_e32 v108, 16, v109
	v_and_b32_e32 v109, 0xffff0000, v109
	v_lshlrev_b32_e32 v134, 16, v110
	v_and_b32_e32 v135, 0xffff0000, v110
	v_lshlrev_b32_e32 v110, 16, v111
	v_and_b32_e32 v111, 0xffff0000, v111
	v_pk_add_f32 v[100:101], v[100:101], v[102:103]
	v_pk_add_f32 v[128:129], v[128:129], v[146:147]
	v_lshlrev_b32_e32 v136, 16, v112
	v_and_b32_e32 v137, 0xffff0000, v112
	v_lshlrev_b32_e32 v112, 16, v113
	v_and_b32_e32 v113, 0xffff0000, v113
	v_lshlrev_b32_e32 v138, 16, v114
	v_and_b32_e32 v139, 0xffff0000, v114
	v_lshlrev_b32_e32 v114, 16, v115
	v_and_b32_e32 v115, 0xffff0000, v115
	v_pk_fma_f32 v[108:109], v[108:109], s[12:13], v[156:157] op_sel_hi:[1,0,1]
	v_pk_fma_f32 v[132:133], v[132:133], s[12:13], v[154:155] op_sel_hi:[1,0,1]
	v_pk_fma_f32 v[110:111], v[110:111], s[12:13], v[160:161] op_sel_hi:[1,0,1]
	v_pk_fma_f32 v[134:135], v[134:135], s[12:13], v[158:159] op_sel_hi:[1,0,1]
	v_pk_add_f32 v[100:101], v[100:101], v[100:101] op_sel:[0,1] op_sel_hi:[1,0]
	v_add_f32_e32 v92, 0, v128
	v_pk_fma_f32 v[112:113], v[112:113], s[12:13], v[164:165] op_sel_hi:[1,0,1]
	v_pk_fma_f32 v[136:137], v[136:137], s[12:13], v[162:163] op_sel_hi:[1,0,1]
	v_pk_fma_f32 v[114:115], v[114:115], s[12:13], v[148:149] op_sel_hi:[1,0,1]
	v_pk_fma_f32 v[140:141], v[140:141], s[12:13], v[144:145] op_sel_hi:[1,0,1]
	v_add_f32_e32 v142, v132, v133
	v_add_f32_e32 v144, v108, v109
	v_mov_b32_e32 v149, v134
	v_mov_b32_e32 v143, v110
	v_mov_b32_e32 v145, v111
	v_mov_b32_e32 v101, v135
	v_add_f32_e32 v148, v92, v129
	v_pk_fma_f32 v[138:139], v[138:139], s[12:13], v[150:151] op_sel_hi:[1,0,1]
	v_pk_mov_b32 v[150:151], v[136:137], v[112:113] op_sel:[1,0]
	v_mov_b32_e32 v152, v136
	v_mov_b32_e32 v153, v113
	v_pk_add_f32 v[102:103], v[142:143], v[144:145]
	v_pk_add_f32 v[100:101], v[148:149], v[100:101]
	v_pk_add_f32 v[142:143], v[150:151], v[152:153]
	v_pk_add_f32 v[100:101], v[100:101], v[102:103]
	v_pk_add_f32 v[142:143], v[142:143], v[142:143] op_sel:[0,1] op_sel_hi:[1,0]
	v_pk_add_f32 v[100:101], v[100:101], v[100:101] op_sel:[0,1] op_sel_hi:[1,0]
	v_add_f32_e32 v154, v138, v139
	v_add_f32_e32 v156, v114, v115
	v_mov_b32_e32 v155, v116
	v_mov_b32_e32 v157, v117
	v_mov_b32_e32 v143, v141
	v_mov_b32_e32 v101, v140
	v_pk_add_f32 v[144:145], v[154:155], v[156:157]
	v_pk_add_f32 v[100:101], v[100:101], v[142:143]
	s_nop 0
	v_pk_add_f32 v[100:101], v[100:101], v[144:145]
	s_nop 0
	v_add_f32_e32 v92, v100, v101
	s_nop 1
	v_add_f32_dpp v92, v92, v92 quad_perm:[1,0,3,2] row_mask:0xf bank_mask:0xf bound_ctrl:1
	s_nop 1
	v_add_f32_dpp v92, v92, v92 quad_perm:[2,3,0,1] row_mask:0xf bank_mask:0xf bound_ctrl:1
	s_nop 1
	v_add_f32_dpp v92, v92, v92 row_half_mirror row_mask:0xf bank_mask:0xf bound_ctrl:1
	s_nop 1
	v_add_f32_dpp v92, v92, v92 row_mirror row_mask:0xf bank_mask:0xf bound_ctrl:1
	s_nop 1
	v_mov_b32_dpp v120, v92 row_bcast:15 row_mask:0xa bank_mask:0xf
	v_add_f32_e32 v92, v92, v120
	s_nop 1
	v_mov_b32_dpp v121, v92 row_bcast:31 row_mask:0xc bank_mask:0xf
	v_add_f32_e32 v92, v92, v121
	s_nop 0
	v_readlane_b32 s2, v92, 63
	s_nop 1
	v_fmac_f32_e32 v97, s2, v118
	v_fmac_f32_e32 v99, s2, v118
	v_fmac_f32_e32 v127, s2, v118
	v_fmac_f32_e32 v125, s2, v118
	v_fma_f32 v96, s2, v118, v96
	v_fma_f32 v98, s2, v118, v98
	v_fma_f32 v126, s2, v118, v126
	v_fma_f32 v124, s2, v118, v124
	v_fmac_f32_e32 v105, s2, v118
	v_fmac_f32_e32 v131, s2, v118
	v_mul_f32_e32 v92, v99, v99
	v_mul_f32_e32 v94, v97, v97
	v_mul_f32_e32 v100, v125, v125
	v_mul_f32_e32 v101, v127, v127
	v_fma_f32 v104, s2, v118, v104
	v_fma_f32 v130, s2, v118, v130
	v_fmac_f32_e32 v109, s2, v118
	v_fmac_f32_e32 v133, s2, v118
	v_mul_f32_e32 v102, v131, v131
	v_mul_f32_e32 v103, v105, v105
	v_fmac_f32_e32 v92, v98, v98
	v_fmac_f32_e32 v94, v96, v96
	v_fmac_f32_e32 v100, v124, v124
	v_fmac_f32_e32 v101, v126, v126
	v_fma_f32 v108, s2, v118, v108
	v_fma_f32 v132, s2, v118, v132
	v_fmac_f32_e32 v111, s2, v118
	v_fmac_f32_e32 v135, s2, v118
	v_mul_f32_e32 v120, v133, v133
	v_mul_f32_e32 v121, v109, v109
	v_fmac_f32_e32 v102, v130, v130
	v_fmac_f32_e32 v103, v104, v104
	v_add_f32_e32 v92, v92, v94
	v_add_f32_e32 v94, v100, v101
	v_fma_f32 v110, s2, v118, v110
	v_fma_f32 v134, s2, v118, v134
	v_fmac_f32_e32 v113, s2, v118
	v_fmac_f32_e32 v137, s2, v118
	v_mul_f32_e32 v128, v135, v135
	v_mul_f32_e32 v129, v111, v111
	v_fmac_f32_e32 v120, v132, v132
	v_fmac_f32_e32 v121, v108, v108
	v_add_f32_e32 v100, v102, v103
	v_add_f32_e32 v92, v92, v94
	v_fma_f32 v112, s2, v118, v112
	v_fma_f32 v136, s2, v118, v136
	v_fmac_f32_e32 v115, s2, v118
	v_fmac_f32_e32 v139, s2, v118
	v_mul_f32_e32 v142, v137, v137
	v_mul_f32_e32 v143, v113, v113
	v_fmac_f32_e32 v128, v134, v134
	v_fmac_f32_e32 v129, v110, v110
	v_add_f32_e32 v101, v120, v121
	v_add_f32_e32 v92, v92, v100
; #define GAS __attribute__((address_space(1)))
; #define LAS __attribute__((address_space(3)))
; __global__ void __launch_bounds__(NTHR, 2) mk_fwd(Args args) {
;     ...
;             const float mean = wave_sum_dpp(s) * (1.0f / D); float s2 = 0.f;
; #pragma unroll
;             for (int q = 0; q < 8; ++q) { v[q] = v[q] - mean; s2 += (v[q].x * v[q].x + v[q].y * v[q].y) + (v[q].z * v[q].z + v[q].w * v[q].w); }
;             const float rstd = 1.0f / sqrtf(wave_sum_dpp(s2) * (1.0f / D) + LN_EPS);
; #pragma unroll
;             for (int q = 0; q < 8; ++q) { const int c = 4 * lane + 256 * q; *(GAS f32x4*)(out + (size_t)m * D + c) = v[q] * rstd * *(const LAS f32x4*)(s_lnw + c) + *(const LAS f32x4*)(s_lnb + c); }
	v_fma_f32 v114, s2, v118, v114
	v_fma_f32 v138, s2, v118, v138
	v_fmac_f32_e32 v117, s2, v118
	v_fmac_f32_e32 v141, s2, v118
	v_mul_f32_e32 v144, v139, v139
	v_mul_f32_e32 v145, v115, v115
	v_fmac_f32_e32 v142, v136, v136
	v_fmac_f32_e32 v143, v112, v112
	v_add_f32_e32 v102, v128, v129
	v_add_f32_e32 v92, v92, v101
	v_fma_f32 v116, s2, v118, v116
	v_fma_f32 v140, s2, v118, v140
	v_mul_f32_e32 v146, v141, v141
	v_mul_f32_e32 v147, v117, v117
	v_fmac_f32_e32 v144, v138, v138
	v_fmac_f32_e32 v145, v114, v114
	v_add_f32_e32 v103, v142, v143
	v_add_f32_e32 v92, v92, v102
	v_fmac_f32_e32 v146, v140, v140
	v_fmac_f32_e32 v147, v116, v116
	v_add_f32_e32 v120, v144, v145
	v_add_f32_e32 v92, v92, v103
	v_add_f32_e32 v121, v146, v147
	v_add_f32_e32 v92, v92, v120
	v_add_f32_e32 v92, v92, v121
	s_nop 1
	v_add_f32_dpp v92, v92, v92 quad_perm:[1,0,3,2] row_mask:0xf bank_mask:0xf bound_ctrl:1
	s_nop 1
	v_add_f32_dpp v92, v92, v92 quad_perm:[2,3,0,1] row_mask:0xf bank_mask:0xf bound_ctrl:1
	s_nop 1
	v_add_f32_dpp v92, v92, v92 row_half_mirror row_mask:0xf bank_mask:0xf bound_ctrl:1
	s_nop 1
	v_add_f32_dpp v92, v92, v92 row_mirror row_mask:0xf bank_mask:0xf bound_ctrl:1
	s_nop 1
	v_mov_b32_dpp v122, v92 row_bcast:15 row_mask:0xa bank_mask:0xf
	v_add_f32_e32 v92, v92, v122
	s_nop 1
	v_mov_b32_dpp v123, v92 row_bcast:31 row_mask:0xc bank_mask:0xf
	v_add_f32_e32 v92, v92, v123
	s_nop 0
	v_readlane_b32 s2, v92, 63
	s_nop 1
	v_fma_f32 v92, s2, v119, v93
	v_mul_f32_e32 v94, 0x4f800000, v92
	v_cmp_gt_f32_e32 vcc, s13, v92
	s_nop 1
	v_cndmask_b32_e32 v92, v92, v94, vcc
	v_sqrt_f32_e32 v94, v92
	s_nop 0
	v_add_u32_e32 v100, -1, v94
	v_add_u32_e32 v101, 1, v94
	v_fma_f32 v102, -v100, v94, v92
	v_fma_f32 v103, -v101, v94, v92
	v_cmp_ge_f32_e64 s[2:3], 0, v102
	s_nop 1
	v_cndmask_b32_e64 v94, v94, v100, s[2:3]
	v_cmp_lt_f32_e64 s[2:3], 0, v103
	s_nop 1
	v_cndmask_b32_e64 v94, v94, v101, s[2:3]
	v_mul_f32_e32 v100, 0x37800000, v94
	v_cndmask_b32_e32 v94, v94, v100, vcc
	v_cmp_class_f32_e32 vcc, v92, v95
	s_nop 1
	v_cndmask_b32_e32 v92, v94, v92, vcc
	v_div_scale_f32 v94, s[2:3], v92, v92, 1.0
	v_rcp_f32_e32 v101, v94
	v_div_scale_f32 v100, vcc, 1.0, v92, 1.0
	v_fma_f32 v102, -v94, v101, 1.0
	v_fmac_f32_e32 v101, v102, v101
	v_mul_f32_e32 v102, v100, v101
	v_fma_f32 v103, -v94, v102, v100
	v_fmac_f32_e32 v102, v103, v101
	v_fma_f32 v94, -v94, v102, v100
	v_div_fmas_f32 v94, v94, v101, v102
	v_div_fixup_f32 v92, v94, v92, 1.0
	v_pk_mul_f32 v[100:101], v[92:93], v[98:99] op_sel_hi:[0,1]
	v_pk_mul_f32 v[96:97], v[92:93], v[96:97] op_sel_hi:[0,1]
	v_pk_mul_f32 v[120:121], v[92:93], v[124:125] op_sel_hi:[0,1]
	v_pk_mul_f32 v[102:103], v[92:93], v[126:127] op_sel_hi:[0,1]
	v_pk_mul_f32 v[122:123], v[92:93], v[130:131] op_sel_hi:[0,1]
	v_pk_mul_f32 v[104:105], v[92:93], v[104:105] op_sel_hi:[0,1]
	v_pk_mul_f32 v[124:125], v[92:93], v[132:133] op_sel_hi:[0,1]
	v_pk_mul_f32 v[126:127], v[92:93], v[108:109] op_sel_hi:[0,1]
	v_pk_mul_f32 v[128:129], v[92:93], v[134:135] op_sel_hi:[0,1]
	v_pk_mul_f32 v[130:131], v[92:93], v[110:111] op_sel_hi:[0,1]
	v_pk_mul_f32 v[132:133], v[92:93], v[136:137] op_sel_hi:[0,1]
	v_pk_mul_f32 v[134:135], v[92:93], v[112:113] op_sel_hi:[0,1]
	v_pk_mul_f32 v[136:137], v[92:93], v[138:139] op_sel_hi:[0,1]
	v_pk_mul_f32 v[138:139], v[92:93], v[114:115] op_sel_hi:[0,1]
	v_pk_mul_f32 v[140:141], v[92:93], v[140:141] op_sel_hi:[0,1]
	v_pk_mul_f32 v[116:117], v[92:93], v[116:117] op_sel_hi:[0,1]
	s_waitcnt lgkmcnt(13)
	v_pk_fma_f32 v[98:99], v[96:97], v[2:3], v[10:11]
	v_pk_fma_f32 v[96:97], v[100:101], v[0:1], v[8:9]
	s_waitcnt lgkmcnt(12)
	v_pk_fma_f32 v[102:103], v[102:103], v[6:7], v[14:15]
	v_pk_fma_f32 v[100:101], v[120:121], v[4:5], v[12:13]
	s_waitcnt lgkmcnt(9)
	v_pk_fma_f32 v[110:111], v[104:105], v[18:19], v[26:27]
	v_pk_fma_f32 v[108:109], v[122:123], v[16:17], v[24:25]
	s_waitcnt lgkmcnt(8)
	v_pk_fma_f32 v[114:115], v[126:127], v[22:23], v[30:31]
	v_pk_fma_f32 v[112:113], v[124:125], v[20:21], v[28:29]
	s_waitcnt lgkmcnt(5)
	v_pk_fma_f32 v[122:123], v[130:131], v[34:35], v[42:43]
	v_pk_fma_f32 v[120:121], v[128:129], v[32:33], v[40:41]
	s_waitcnt lgkmcnt(4)
	v_pk_fma_f32 v[126:127], v[134:135], v[38:39], v[46:47]
	v_pk_fma_f32 v[124:125], v[132:133], v[36:37], v[44:45]
	s_waitcnt lgkmcnt(1)
	v_pk_fma_f32 v[130:131], v[138:139], v[50:51], v[58:59]
	v_pk_fma_f32 v[128:129], v[136:137], v[48:49], v[56:57]
	s_waitcnt lgkmcnt(0)
	v_pk_fma_f32 v[134:135], v[116:117], v[54:55], v[62:63]
	v_pk_fma_f32 v[132:133], v[140:141], v[52:53], v[60:61]
	global_store_dwordx4 v[106:107], v[96:99], off offset:-3072 nt
	global_store_dwordx4 v[106:107], v[100:103], off offset:-2048 nt
	global_store_dwordx4 v[106:107], v[108:111], off offset:-1024 nt
	global_store_dwordx4 v[88:89], v[112:115], off offset:-4096 nt
	global_store_dwordx4 v[88:89], v[120:123], off offset:-3072 nt
	global_store_dwordx4 v[88:89], v[124:127], off offset:-2048 nt
	global_store_dwordx4 v[88:89], v[128:131], off offset:-1024 nt
	global_store_dwordx4 v[88:89], v[132:135], off nt
	v_lshl_add_u64 v[88:89], v[88:89], 0, s[6:7]
	s_mov_b64 vcc, s[0:1]
	s_cbranch_vccnz .LBB0_1219
